# speedup vs baseline: 1.1068x; 1.0029x over previous
.LBB5_15:
	s_or_b64 exec, exec, s[6:7]
	s_load_dwordx4 s[4:7], s[0:1], 0x18
	v_mov_b32_e32 v17, 0
	s_waitcnt lgkmcnt(0)
	s_barrier
	ds_read_b32 v17, v17 offset:32776
	s_and_b32 s17, s5, 0xffff
	s_and_b32 s21, s15, 0xffff
	v_accvgpr_read_b32 v56, a0
	v_lshlrev_b32_e32 v15, 12, v1
	v_lshlrev_b32_e32 v18, 4, v56
	s_add_u32 s8, s4, s7
	s_mov_b32 s16, s4
	v_lshlrev_b32_e32 v14, 14, v10
	v_lshlrev_b32_e32 v16, 7, v0
	s_addc_u32 s9, s5, 0
	s_waitcnt lgkmcnt(0)
	v_cmp_ne_u32_e64 s[4:5], 0, v17
	v_add_u32_e32 v17, 0, v15
	v_or_b32_e32 v15, v18, v15
	v_or3_b32 v15, v16, v14, v15
	v_lshlrev_b32_e32 v13, 3, v0
	v_accvgpr_write_b32 a98, v15
	v_and_b32_e32 v15, 63, v57
	v_lshlrev_b32_e32 v19, 4, v13
	v_lshrrev_b32_e32 v15, 5, v15
	s_waitcnt vmcnt(1)
	v_mul_f32_e32 v45, 0xbfb8aa3b, v6
	v_mul_f32_e32 v6, 0xbfb8aa3b, v7
	v_mul_f32_e32 v7, 0xbfb8aa3b, v9
	v_lshlrev_b32_e32 v9, 8, v1
	v_add3_u32 v17, v17, v19, v18
	v_accvgpr_write_b32 a94, v15
	v_bfe_u32 v16, v57, 2, 3
	v_lshlrev_b32_e32 v15, 3, v57
	v_add_u32_e32 v9, v23, v9
	v_accvgpr_write_b32 a97, v17
	v_and_b32_e32 v17, 24, v15
	v_lshlrev_b32_e32 v10, 13, v10
	v_lshlrev_b32_e32 v15, 10, v16
	v_or_b32_e32 v9, v9, v13
	v_or3_b32 v10, v10, v15, v17
	v_cmp_eq_u32_e64 s[2:3], 3, v1
	v_lshl_add_u32 v9, v9, 1, s6
	v_accvgpr_write_b32 a95, v16
	v_lshl_add_u32 v16, v10, 1, s44
	v_lshlrev_b32_e32 v1, 7, v1
	v_and_b32_e32 v10, 8, v57
	v_lshlrev_b32_e32 v0, 1, v0
	v_or3_b32 v1, v1, v10, v0
	v_add_u32_e32 v10, s24, v9
	s_lshl_b32 s6, s33, 9
	v_or3_b32 v1, v1, v18, v14
	v_accvgpr_write_b32 a99, v10
	v_add_u32_e32 v10, s26, v9
	v_add_u32_e32 v1, s6, v1
	s_and_b32 s33, s6, 0xe00
	s_lshl_b32 s6, s42, 9
	v_accvgpr_write_b32 a102, v10
	v_add_u32_e32 v10, s28, v9
	s_and_b32 s35, s6, 0xe00
	s_lshl_b32 s6, s43, 9
	v_accvgpr_write_b32 a103, v10
	v_add_u32_e32 v10, s30, v9
	s_and_b32 s37, s6, 0xe00
	s_lshl_b32 s6, s45, 9
	v_accvgpr_write_b32 a104, v10
	v_add_u32_e32 v10, s34, v9
	v_accvgpr_write_b32 a96, v17
	v_ashrrev_i32_e32 v17, 31, v16
	s_and_b32 s39, s6, 0xe00
	s_lshl_b32 s6, s46, 9
	v_accvgpr_write_b32 a105, v10
	v_add_u32_e32 v10, s36, v9
	v_accvgpr_write_b32 a93, v17
	s_and_b32 s41, s6, 0xe00
	s_lshl_b32 s6, s47, 9
	v_accvgpr_write_b32 a106, v10
	v_add_u32_e32 v10, s38, v9
	v_add_u32_e32 v9, s40, v9
	v_or_b32_e32 v13, v13, v56
	v_accvgpr_write_b32 a92, v16
	v_lshl_add_u64 v[16:17], s[8:9], 0, v[16:17]
	s_and_b32 s42, s6, 0xe00
	s_lshl_b32 s6, s48, 9
	v_accvgpr_write_b32 a108, v9
	v_lshlrev_b32_e32 v9, 1, v12
	s_mov_b32 s19, 0x20000
	v_accvgpr_write_b32 a101, v17
	s_and_b32 s43, s6, 0xe00
	s_lshl_b32 s6, s49, 9
	v_accvgpr_write_b32 a107, v10
	v_add3_u32 v0, 0, v9, v0
	v_lshlrev_b32_e32 v9, 9, v11
	v_lshlrev_b32_e32 v10, 4, v13
	s_brev_b32 s18, -2
	s_mov_b32 s22, 0x80000
	s_mov_b32 s23, s19
	s_mov_b32 s20, s14
	v_cmp_gt_u32_e64 s[0:1], 8, v22
	s_mov_b32 s15, 0
	v_accvgpr_write_b32 a100, v16
	s_and_b32 s44, s6, 0xe00
	v_add3_u32 v9, 0, v9, v10
	s_mov_b64 s[26:27], 0
	s_mov_b32 s34, 0x80008000
	s_mov_b32 s36, 0x100000
	s_brev_b32 s38, 60
	s_mov_b32 s40, 0xbc38aa3b
	s_mov_b32 s45, 0x41000000
	s_waitcnt vmcnt(0)
	v_accvgpr_write_b32 a112, v250
	v_accvgpr_write_b32 a113, v251
	v_accvgpr_write_b32 a114, v252
	v_accvgpr_write_b32 a115, v253
	v_accvgpr_write_b32 a116, v2
	v_accvgpr_write_b32 a117, v3
	v_accvgpr_write_b32 a118, v4
	v_accvgpr_write_b32 a119, v5
	v_and_b32_e32 v46, 8, v57
	v_cmp_ne_u32_e64 s[0:1], 0, v46
	v_and_b32_e32 v46, 32, v57
	v_cmp_ne_u32_e64 s[30:31], 0, v46
	v_mov_b32_e32 v26, 0x44444444
	v_mov_b32_e32 v46, 0xeeeeeeee
	v_cndmask_b32_e64 v26, v26, v46, s[0:1]
	v_accvgpr_read_b32 v46, a98
	v_bfe_u32 v47, v57, 4, 2
	v_lshlrev_b32_e32 v47, 7, v47
	v_sub_u32_e32 v46, v46, v47
	v_bfe_u32 v47, v57, 4, 1
	v_bfe_u32 v48, v57, 3, 1
	v_lshl_or_b32 v47, v47, 1, v48
	v_lshl_add_u32 v46, v47, 7, v46
	v_mov_b32_e32 v47, s33
	v_mov_b32_e32 v48, s35
	v_cndmask_b32_e64 v47, v47, v48, s[30:31]
	v_or_b32_e32 v27, v46, v47
	v_mov_b32_e32 v47, s37
	v_mov_b32_e32 v48, s39
	v_cndmask_b32_e64 v47, v47, v48, s[30:31]
	v_or_b32_e32 v28, v46, v47
	v_mov_b32_e32 v47, s41
	v_mov_b32_e32 v48, s42
	v_cndmask_b32_e64 v47, v47, v48, s[30:31]
	v_or_b32_e32 v29, v46, v47
	v_mov_b32_e32 v47, s43
	v_mov_b32_e32 v48, s44
	v_cndmask_b32_e64 v47, v47, v48, s[30:31]
	v_or_b32_e32 v30, v46, v47
	v_lshrrev_b32_e32 v46, 6, v57
	v_lshlrev_b32_e32 v46, 7, v46
	v_and_b32_e32 v47, 8, v57
	v_bfe_u32 v48, v57, 4, 2
	v_lshl_or_b32 v47, v48, 1, v47
	v_add_u32_e32 v46, v46, v47
	v_sub_u32_e32 v1, v1, v46
	v_bfe_u32 v46, v57, 7, 1
	v_bfe_u32 v47, v57, 5, 1
	v_lshl_or_b32 v46, v46, 1, v47
	v_lshlrev_b32_e32 v46, 7, v46
	v_bfe_u32 v47, v57, 3, 1
	v_bfe_u32 v48, v57, 6, 1
	v_lshl_or_b32 v47, v48, 1, v47
	v_lshl_or_b32 v46, v47, 2, v46
	v_bfe_u32 v47, v57, 4, 1
	v_lshl_or_b32 v46, v47, 1, v46
	v_add_u32_e32 v1, v1, v46
	v_lshrrev_b32_e32 v46, 6, v57
	v_lshlrev_b32_e32 v46, 12, v46
	v_and_b32_e32 v47, 16, v57
	v_lshl_or_b32 v46, v47, 7, v46
	v_lshl_or_b32 v46, v47, 3, v46
	v_and_b32_e32 v47, 32, v57
	v_lshl_or_b32 v46, v47, 3, v46
	v_and_b32_e32 v47, 3, v57
	v_lshl_or_b32 v46, v47, 2, v46
	v_bfe_u32 v47, v57, 2, 2
	v_xor_b32_e32 v48, 0, v47
	v_lshl_or_b32 v48, v48, 4, v46
	v_add_u32_e32 v31, 0, v48
	v_xor_b32_e32 v35, 0x80, v31
	v_xor_b32_e32 v48, 1, v47
	v_lshl_or_b32 v48, v48, 4, v46
	v_add_u32_e32 v32, 512, v48
	v_xor_b32_e32 v36, 0x80, v32
	v_xor_b32_e32 v48, 2, v47
	v_lshl_or_b32 v48, v48, 4, v46
	v_add_u32_e32 v33, 1024, v48
	v_xor_b32_e32 v37, 0x80, v33
	v_xor_b32_e32 v48, 3, v47
	v_lshl_or_b32 v48, v48, 4, v46
	v_add_u32_e32 v34, 1536, v48
	v_xor_b32_e32 v38, 0x80, v34
	v_lshrrev_b32_e32 v46, 3, v57
	v_and_b32_e32 v46, 24, v46
	v_lshrrev_b32_e32 v47, 1, v57
	v_and_or_b32 v46, v47, 4, v46
	v_bfe_u32 v47, v57, 4, 2
	v_or_b32_e32 v46, v46, v47
	v_and_b32_e32 v47, 3, v57
	v_and_b32_e32 v48, 4, v57
	v_lshl_or_b32 v47, v48, 1, v47
	v_xor_b32_e32 v46, v46, v47
	v_and_b32_e32 v47, 7, v57
	v_lshlrev_b32_e32 v47, 9, v47
	v_lshl_or_b32 v9, v46, 4, v47
	v_accvgpr_write_b32 a120, v226
	v_accvgpr_write_b32 a121, v227
	v_accvgpr_write_b32 a122, v228
	v_accvgpr_write_b32 a123, v229
	v_accvgpr_write_b32 a124, v230
	v_accvgpr_write_b32 a125, v231
	v_accvgpr_write_b32 a126, v232
	v_accvgpr_write_b32 a127, v233
	v_accvgpr_write_b32 a128, v234
	v_accvgpr_write_b32 a129, v235
	v_accvgpr_write_b32 a130, v236
	v_accvgpr_write_b32 a131, v237
	v_accvgpr_write_b32 a132, v238
	v_accvgpr_write_b32 a133, v239
	v_accvgpr_write_b32 a134, v240
	v_accvgpr_write_b32 a135, v241
	v_accvgpr_write_b32 a136, v242
	v_accvgpr_write_b32 a137, v243
	v_accvgpr_write_b32 a138, v244
	v_accvgpr_write_b32 a139, v245
	v_accvgpr_write_b32 a140, v246
	v_accvgpr_write_b32 a141, v247
	v_accvgpr_write_b32 a142, v248
	v_accvgpr_write_b32 a143, v249
	v_accvgpr_write_b32 a144, v194
	v_accvgpr_write_b32 a145, v195
	v_accvgpr_write_b32 a146, v196
	v_accvgpr_write_b32 a147, v197
	v_accvgpr_write_b32 a148, v198
	v_accvgpr_write_b32 a149, v199
	v_accvgpr_write_b32 a150, v200
	v_accvgpr_write_b32 a151, v201
	v_accvgpr_write_b32 a152, v202
	v_accvgpr_write_b32 a153, v203
	v_accvgpr_write_b32 a154, v204
	v_accvgpr_write_b32 a155, v205
	v_accvgpr_write_b32 a156, v206
	v_accvgpr_write_b32 a157, v207
	v_accvgpr_write_b32 a158, v208
	v_accvgpr_write_b32 a159, v209
	v_accvgpr_write_b32 a160, v210
	v_accvgpr_write_b32 a161, v211
	v_accvgpr_write_b32 a162, v212
	v_accvgpr_write_b32 a163, v213
	v_accvgpr_write_b32 a164, v214
	v_accvgpr_write_b32 a165, v215
	v_accvgpr_write_b32 a166, v216
	v_accvgpr_write_b32 a167, v217
	v_accvgpr_write_b32 a168, v218
	v_accvgpr_write_b32 a169, v219
	v_accvgpr_write_b32 a170, v220
	v_accvgpr_write_b32 a171, v221
	v_accvgpr_write_b32 a172, v222
	v_accvgpr_write_b32 a173, v223
	v_accvgpr_write_b32 a174, v224
	v_accvgpr_write_b32 a175, v225
	s_mov_b64 s[24:25], 0
	s_mov_b32 s46, 0
	s_mov_b32 s30, 0x3c38aa3b
	s_mov_b32 s31, 0xbc000000
	v_bfe_u32 v50, v57, 4, 2
	v_lshlrev_b32_e32 v50, 4, v50
	v_bfe_u32 v51, v57, 4, 1
	v_bfe_u32 v52, v57, 3, 1
	v_lshlrev_b32_e32 v52, 2, v52
	v_lshl_or_b32 v51, v51, 5, v52
	v_sub_u32_e32 v54, v51, v50
	v_and_b32_e32 v55, 32, v57
	v_cmp_ne_u32_e64 s[28:29], 0, v55
	v_accvgpr_read_b32 v242, a99
	v_accvgpr_read_b32 v55, a102
	v_cndmask_b32_e64 v242, v242, v55, s[28:29]
	v_add_u32_e32 v242, v242, v54
	v_accvgpr_read_b32 v243, a103
	v_accvgpr_read_b32 v55, a104
	v_cndmask_b32_e64 v243, v243, v55, s[28:29]
	v_add_u32_e32 v243, v243, v54
	v_accvgpr_read_b32 v244, a105
	v_accvgpr_read_b32 v55, a106
	v_cndmask_b32_e64 v244, v244, v55, s[28:29]
	v_add_u32_e32 v244, v244, v54
	v_accvgpr_read_b32 v245, a107
	v_accvgpr_read_b32 v55, a108
	v_cndmask_b32_e64 v245, v245, v55, s[28:29]
	v_add_u32_e32 v245, v245, v54
	s_mov_b64 s[26:27], -1
	v_mov_b32_e32 v10, 0
	v_mov_b32_e32 v11, 0
	v_mov_b32_e32 v12, 0
	v_mov_b32_e32 v13, 0
	v_mov_b32_e32 v14, 0
	v_mov_b32_e32 v15, 0
	v_mov_b32_e32 v16, 0
	v_mov_b32_e32 v17, 0
	v_mov_b32_e32 v18, 0
	v_mov_b32_e32 v19, 0
	v_mov_b32_e32 v20, 0
	v_mov_b32_e32 v21, 0
	v_mov_b32_e32 v22, 0
	v_mov_b32_e32 v23, 0
	v_mov_b32_e32 v24, 0
	v_mov_b32_e32 v25, 0
	v_mov_b32_e32 v2, 0
	v_mov_b32_e32 v3, 0
	v_mov_b32_e32 v4, 0
	v_mov_b32_e32 v5, 0
	v_mov_b32_e32 v250, 0
	v_mov_b32_e32 v251, 0
	v_mov_b32_e32 v252, 0
	v_mov_b32_e32 v253, 0
	v_mov_b32_e32 v46, 0
	v_mov_b32_e32 v47, 0
	v_mov_b32_e32 v48, 0
	v_mov_b32_e32 v49, 0
	v_mov_b32_e32 v50, 0
	v_mov_b32_e32 v51, 0
	v_mov_b32_e32 v52, 0
	v_mov_b32_e32 v53, 0
	buffer_load_dword v226, v242, s[16:19], 0 offen sc1
	buffer_load_dword v227, v242, s[16:19], 0 offen offset:8 sc1
	buffer_load_dword v228, v242, s[16:19], 0 offen offset:16 sc1
	buffer_load_dword v229, v242, s[16:19], 0 offen offset:24 sc1
	buffer_load_dword v230, v243, s[16:19], 0 offen sc1
	buffer_load_dword v231, v243, s[16:19], 0 offen offset:8 sc1
	buffer_load_dword v232, v243, s[16:19], 0 offen offset:16 sc1
	buffer_load_dword v233, v243, s[16:19], 0 offen offset:24 sc1
	buffer_load_dword v234, v244, s[16:19], 0 offen sc1
	buffer_load_dword v235, v244, s[16:19], 0 offen offset:8 sc1
	buffer_load_dword v236, v244, s[16:19], 0 offen offset:16 sc1
	buffer_load_dword v237, v244, s[16:19], 0 offen offset:24 sc1
	buffer_load_dword v238, v245, s[16:19], 0 offen sc1
	buffer_load_dword v239, v245, s[16:19], 0 offen offset:8 sc1
	buffer_load_dword v240, v245, s[16:19], 0 offen offset:16 sc1
	buffer_load_dword v241, v245, s[16:19], 0 offen offset:24 sc1
	s_waitcnt vmcnt(0)
.Lrec_step:
	s_bitcmp0_b32 s46, 2
	s_cselect_b32 s28, 0, s34
	s_cselect_b32 s47, s38, s31
	s_cselect_b32 s48, s40, s30
	s_mov_b32 s14, 0
	s_waitcnt vmcnt(9)
	s_cmp_eq_u32 s46, 0
	s_cbranch_scc1 .Lrec_norot
	v_accvgpr_read_b32 v43, a33
	v_accvgpr_read_b32 v42, a32
	v_accvgpr_write_b32 a33, v41
	v_accvgpr_write_b32 a32, v40

.Lrec_a0:
	s_waitcnt vmcnt(7)
	v_bitop3_b32 v54, v226, v227, s28 bitop3:0x7e
	v_bitop3_b32 v55, v228, v229, s28 bitop3:0x7e
	v_bitop3_b32 v54, v54, v55, s34 bitop3:0xa8
	v_cmp_ne_u32_e32 vcc, 0, v54
	s_andn2_b64 vcc, vcc, s[26:27]
	s_cbranch_vccnz .Lrec_b0
	v_smfmac_f32_16x16x64_f16 v[10:13], v[226:229], a[36:43], v26
	v_smfmac_f32_16x16x64_f16 v[14:17], v[226:229], a[68:75], v26
	v_smfmac_f32_16x16x64_f16 v[18:21], v[226:229], v[66:73], v26
	v_smfmac_f32_16x16x64_f16 v[22:25], v[226:229], v[98:105], v26
	v_smfmac_f32_16x16x64_f16 v[46:49], v[226:229], v[130:137], v26
	v_smfmac_f32_16x16x64_f16 v[50:53], v[226:229], v[162:169], v26
	v_smfmac_f32_16x16x64_f16 v[2:5], v[226:229], a[144:151], v26
	v_smfmac_f32_16x16x64_f16 v[250:253], v[226:229], a[120:127], v26
.Lrec_a1:
	s_waitcnt vmcnt(6)
	v_bitop3_b32 v54, v230, v231, s28 bitop3:0x7e
	v_bitop3_b32 v55, v232, v233, s28 bitop3:0x7e
	v_bitop3_b32 v54, v54, v55, s34 bitop3:0xa8
	v_cmp_ne_u32_e32 vcc, 0, v54
	s_andn2_b64 vcc, vcc, s[26:27]
	s_cbranch_vccnz .Lrec_b1
	v_smfmac_f32_16x16x64_f16 v[10:13], v[230:233], a[44:51], v26
	v_smfmac_f32_16x16x64_f16 v[14:17], v[230:233], a[76:83], v26
	v_smfmac_f32_16x16x64_f16 v[18:21], v[230:233], v[74:81], v26
	v_smfmac_f32_16x16x64_f16 v[22:25], v[230:233], v[106:113], v26
	v_smfmac_f32_16x16x64_f16 v[46:49], v[230:233], v[138:145], v26
	v_smfmac_f32_16x16x64_f16 v[50:53], v[230:233], v[170:177], v26
	v_smfmac_f32_16x16x64_f16 v[2:5], v[230:233], a[152:159], v26
	v_smfmac_f32_16x16x64_f16 v[250:253], v[230:233], a[128:135], v26
.Lrec_a2:
	s_waitcnt vmcnt(5)
	v_bitop3_b32 v54, v234, v235, s28 bitop3:0x7e
	v_bitop3_b32 v55, v236, v237, s28 bitop3:0x7e
	v_bitop3_b32 v54, v54, v55, s34 bitop3:0xa8
	v_cmp_ne_u32_e32 vcc, 0, v54
	s_andn2_b64 vcc, vcc, s[26:27]
	s_cbranch_vccnz .Lrec_b2
	v_smfmac_f32_16x16x64_f16 v[10:13], v[234:237], a[52:59], v26
	v_smfmac_f32_16x16x64_f16 v[14:17], v[234:237], a[84:91], v26
	v_smfmac_f32_16x16x64_f16 v[18:21], v[234:237], v[82:89], v26
	v_smfmac_f32_16x16x64_f16 v[22:25], v[234:237], v[114:121], v26
	v_smfmac_f32_16x16x64_f16 v[46:49], v[234:237], v[146:153], v26
	v_smfmac_f32_16x16x64_f16 v[50:53], v[234:237], v[178:185], v26
	v_smfmac_f32_16x16x64_f16 v[2:5], v[234:237], a[160:167], v26
	v_smfmac_f32_16x16x64_f16 v[250:253], v[234:237], a[136:143], v26
.Lrec_a3:
	s_waitcnt vmcnt(4)
	v_bitop3_b32 v54, v238, v239, s28 bitop3:0x7e
	v_bitop3_b32 v55, v240, v241, s28 bitop3:0x7e
	v_bitop3_b32 v54, v54, v55, s34 bitop3:0xa8
	v_cmp_ne_u32_e32 vcc, 0, v54
	s_andn2_b64 vcc, vcc, s[26:27]
	s_cbranch_vccnz .Lrec_b3
	v_smfmac_f32_16x16x64_f16 v[10:13], v[238:241], a[60:67], v26
	v_smfmac_f32_16x16x64_f16 v[14:17], v[238:241], v[58:65], v26
	v_smfmac_f32_16x16x64_f16 v[18:21], v[238:241], v[90:97], v26
	v_smfmac_f32_16x16x64_f16 v[22:25], v[238:241], v[122:129], v26
	v_smfmac_f32_16x16x64_f16 v[46:49], v[238:241], v[154:161], v26
	v_smfmac_f32_16x16x64_f16 v[50:53], v[238:241], v[186:193], v26
	v_smfmac_f32_16x16x64_f16 v[2:5], v[238:241], a[168:175], v26
	v_smfmac_f32_16x16x64_f16 v[250:253], v[238:241], a[112:119], v26
	s_branch .Lrec_tail
.Lrec_b0:
	s_waitcnt vmcnt(3)
	v_bitop3_b32 v54, v194, v195, s28 bitop3:0x7e
	v_bitop3_b32 v55, v196, v197, s28 bitop3:0x7e
	v_bitop3_b32 v54, v54, v55, s34 bitop3:0xa8
	v_cmp_ne_u32_e32 vcc, 0, v54
	s_andn2_b64 vcc, vcc, s[26:27]
	s_cbranch_vccnz .Lrec_retry0
	v_smfmac_f32_16x16x64_f16 v[10:13], v[194:197], a[36:43], v26
	v_smfmac_f32_16x16x64_f16 v[14:17], v[194:197], a[68:75], v26
	v_smfmac_f32_16x16x64_f16 v[18:21], v[194:197], v[66:73], v26
	v_smfmac_f32_16x16x64_f16 v[22:25], v[194:197], v[98:105], v26
	v_smfmac_f32_16x16x64_f16 v[46:49], v[194:197], v[130:137], v26
	v_smfmac_f32_16x16x64_f16 v[50:53], v[194:197], v[162:169], v26
	v_smfmac_f32_16x16x64_f16 v[2:5], v[194:197], a[144:151], v26
	v_smfmac_f32_16x16x64_f16 v[250:253], v[194:197], a[120:127], v26
.Lrec_b1:
	s_waitcnt vmcnt(2)
	v_bitop3_b32 v54, v198, v199, s28 bitop3:0x7e
	v_bitop3_b32 v55, v200, v201, s28 bitop3:0x7e
	v_bitop3_b32 v54, v54, v55, s34 bitop3:0xa8
	v_cmp_ne_u32_e32 vcc, 0, v54
	s_andn2_b64 vcc, vcc, s[26:27]
	s_cbranch_vccnz .Lrec_retry1
	v_smfmac_f32_16x16x64_f16 v[10:13], v[198:201], a[44:51], v26
	v_smfmac_f32_16x16x64_f16 v[14:17], v[198:201], a[76:83], v26
	v_smfmac_f32_16x16x64_f16 v[18:21], v[198:201], v[74:81], v26
	v_smfmac_f32_16x16x64_f16 v[22:25], v[198:201], v[106:113], v26
	v_smfmac_f32_16x16x64_f16 v[46:49], v[198:201], v[138:145], v26
	v_smfmac_f32_16x16x64_f16 v[50:53], v[198:201], v[170:177], v26
	v_smfmac_f32_16x16x64_f16 v[2:5], v[198:201], a[152:159], v26
	v_smfmac_f32_16x16x64_f16 v[250:253], v[198:201], a[128:135], v26
.Lrec_b2:
	s_waitcnt vmcnt(1)
	v_bitop3_b32 v54, v202, v203, s28 bitop3:0x7e
	v_bitop3_b32 v55, v204, v205, s28 bitop3:0x7e
	v_bitop3_b32 v54, v54, v55, s34 bitop3:0xa8
	v_cmp_ne_u32_e32 vcc, 0, v54
	s_andn2_b64 vcc, vcc, s[26:27]
	s_cbranch_vccnz .Lrec_retry2
	v_smfmac_f32_16x16x64_f16 v[10:13], v[202:205], a[52:59], v26
	v_smfmac_f32_16x16x64_f16 v[14:17], v[202:205], a[84:91], v26
	v_smfmac_f32_16x16x64_f16 v[18:21], v[202:205], v[82:89], v26
	v_smfmac_f32_16x16x64_f16 v[22:25], v[202:205], v[114:121], v26
	v_smfmac_f32_16x16x64_f16 v[46:49], v[202:205], v[146:153], v26
	v_smfmac_f32_16x16x64_f16 v[50:53], v[202:205], v[178:185], v26
	v_smfmac_f32_16x16x64_f16 v[2:5], v[202:205], a[160:167], v26
	v_smfmac_f32_16x16x64_f16 v[250:253], v[202:205], a[136:143], v26
.Lrec_b3:
	s_waitcnt vmcnt(0)
	v_bitop3_b32 v54, v206, v207, s28 bitop3:0x7e
	v_bitop3_b32 v55, v208, v209, s28 bitop3:0x7e
	v_bitop3_b32 v54, v54, v55, s34 bitop3:0xa8
	v_cmp_ne_u32_e32 vcc, 0, v54
	s_andn2_b64 vcc, vcc, s[26:27]
	s_cbranch_vccnz .Lrec_retry3
	v_smfmac_f32_16x16x64_f16 v[10:13], v[206:209], a[60:67], v26
	v_smfmac_f32_16x16x64_f16 v[14:17], v[206:209], v[58:65], v26
	v_smfmac_f32_16x16x64_f16 v[18:21], v[206:209], v[90:97], v26
	v_smfmac_f32_16x16x64_f16 v[22:25], v[206:209], v[122:129], v26
	v_smfmac_f32_16x16x64_f16 v[46:49], v[206:209], v[154:161], v26
	v_smfmac_f32_16x16x64_f16 v[50:53], v[206:209], v[186:193], v26
	v_smfmac_f32_16x16x64_f16 v[2:5], v[206:209], a[168:175], v26
	v_smfmac_f32_16x16x64_f16 v[250:253], v[206:209], a[112:119], v26
.Lrec_tail:
	s_add_i32 s14, s46, 1
	s_lshl_b32 s6, s14, 13
	s_lshl_b32 s7, s14, 17
	s_and_b32 s6, s6, 0x8000
	s_and_b32 s7, s7, 0x60000
	v_add_u32_e32 v242, s7, v27
	v_add_u32_e32 v243, s7, v28
	v_add_u32_e32 v244, s7, v29
	v_add_u32_e32 v245, s7, v30
	v_permlane32_swap_b32_e32 v10, v46
	v_permlane32_swap_b32_e32 v14, v50
	v_permlane32_swap_b32_e32 v18, v2
	v_permlane32_swap_b32_e32 v22, v250
	v_add_f32_e32 v10, v10, v46
	v_add_f32_e32 v14, v14, v50
	v_add_f32_e32 v18, v18, v2
	v_add_f32_e32 v22, v22, v250
	ds_write_b32 v31, v10
	ds_write_b32 v31, v14 offset:64
	ds_write_b32 v35, v18
	ds_write_b32 v35, v22 offset:64
	v_permlane32_swap_b32_e32 v11, v47
	v_permlane32_swap_b32_e32 v15, v51
	v_permlane32_swap_b32_e32 v19, v3
	v_permlane32_swap_b32_e32 v23, v251
	v_add_f32_e32 v11, v11, v47
	v_add_f32_e32 v15, v15, v51
	v_add_f32_e32 v19, v19, v3
	v_add_f32_e32 v23, v23, v251
	ds_write_b32 v32, v11
	ds_write_b32 v32, v15 offset:64
	ds_write_b32 v36, v19
	ds_write_b32 v36, v23 offset:64
	v_permlane32_swap_b32_e32 v12, v48
	v_permlane32_swap_b32_e32 v16, v52
	v_permlane32_swap_b32_e32 v20, v4
	v_permlane32_swap_b32_e32 v24, v252
	v_add_f32_e32 v12, v12, v48
	v_add_f32_e32 v16, v16, v52
	v_add_f32_e32 v20, v20, v4
	v_add_f32_e32 v24, v24, v252
	ds_write_b32 v33, v12
	ds_write_b32 v33, v16 offset:64
	ds_write_b32 v37, v20
	ds_write_b32 v37, v24 offset:64
	v_permlane32_swap_b32_e32 v13, v49
	v_permlane32_swap_b32_e32 v17, v53
	v_permlane32_swap_b32_e32 v21, v5
	v_permlane32_swap_b32_e32 v25, v253
	v_add_f32_e32 v13, v13, v49
	v_add_f32_e32 v17, v17, v53
	v_add_f32_e32 v21, v21, v5
	v_add_f32_e32 v25, v25, v253
	ds_write_b32 v34, v13
	ds_write_b32 v34, v17 offset:64
	ds_write_b32 v38, v21
	ds_write_b32 v38, v25 offset:64
	s_waitcnt lgkmcnt(0)
	s_barrier
	ds_read_b128 v[10:13], v9
	ds_read_b128 v[14:17], v9 offset:4096
	ds_read_b128 v[18:21], v9 offset:8192
	ds_read_b128 v[22:25], v9 offset:12288
	s_min_u32 s29, s46, 0xfd
	s_lshl_b32 s29, s29, 19
	s_add_u32 s29, s29, s36
	v_mov_b32_e32 v54, s29
	v_add_co_u32_e32 v54, vcc, v254, v54
	s_nop 1
	v_addc_co_u32_e32 v55, vcc, 0, v255, vcc
	global_load_dwordx2 v[40:41], v[54:55], off
	s_waitcnt lgkmcnt(2)
	v_pk_add_f32 v[10:11], v[10:11], v[14:15]
	v_pk_add_f32 v[12:13], v[12:13], v[16:17]
	s_waitcnt lgkmcnt(0)
	v_pk_add_f32 v[18:19], v[18:19], v[22:23]
	v_pk_add_f32 v[20:21], v[20:21], v[24:25]
	v_pk_add_f32 v[10:11], v[10:11], v[18:19]
	v_pk_add_f32 v[12:13], v[12:13], v[20:21]
	v_fmac_f32_e32 v247, s48, v11
	v_fmac_f32_e32 v246, s48, v10
	v_fmac_f32_e32 v249, s48, v13
	v_fmac_f32_e32 v248, s47, v12
	v_exp_f32_e32 v15, v247
	v_exp_f32_e32 v14, v246
	v_exp_f32_e32 v17, v249
	v_max_f32_e32 v16, 0, v248
	v_add_f32_e32 v15, 1.0, v15
	v_add_f32_e32 v14, 1.0, v14
	v_add_f32_e32 v17, 1.0, v17
	v_rcp_f32_e32 v14, v14
	v_rcp_f32_e32 v15, v15
	v_rcp_f32_e32 v17, v17
	v_add_u32_e32 v18, s7, v1
	v_mul_f32_e32 v12, v16, v14
	v_fmac_f32_e32 v12, v44, v15
	v_max_f32_e32 v19, 0, v12
	v_mul_f32_e32 v13, v17, v19
	v_fma_mixlo_f16 v14, v13, s45, 0
	s_lshl_b32 s29, s46, 3
	v_and_b32_e32 v14, 0x7fff, v14
	s_andn2_b64 vcc, exec, s[4:5]
	v_or_b32_e32 v16, s6, v14
	s_cbranch_vccnz .Lrec_slowst
	buffer_store_short v16, v18, s[20:23], 0 offen
	s_branch .Lrec_stored

.Lrec_stored:
	s_cmpk_eq_i32 s14, 0x100
	s_cbranch_scc1 .Lrec_exit
	v_and_or_b32 v15, s29, 56, v56
	v_lshl_add_u32 v15, v15, 6, v0
	ds_write_b16 v15, v14 offset:33024
	v_mov_b32_e32 v44, v12
	v_xor_b32_e32 v31, 0x4000, v31
	v_xor_b32_e32 v32, 0x4000, v32
	v_xor_b32_e32 v33, 0x4000, v33
	v_xor_b32_e32 v34, 0x4000, v34
	v_xor_b32_e32 v35, 0x4000, v35
	v_xor_b32_e32 v36, 0x4000, v36
	v_xor_b32_e32 v37, 0x4000, v37
	v_xor_b32_e32 v38, 0x4000, v38
	v_xor_b32_e32 v9, 0x4000, v9
	v_mov_b32_e32 v10, 0
	v_mov_b32_e32 v11, 0
	v_mov_b32_e32 v12, 0
	v_mov_b32_e32 v13, 0
	v_mov_b32_e32 v14, 0
	v_mov_b32_e32 v15, 0
	v_mov_b32_e32 v16, 0
	v_mov_b32_e32 v17, 0
	v_mov_b32_e32 v18, 0
	v_mov_b32_e32 v19, 0
	v_mov_b32_e32 v20, 0
	v_mov_b32_e32 v21, 0
	v_mov_b32_e32 v22, 0
	v_mov_b32_e32 v23, 0
	v_mov_b32_e32 v24, 0
	v_mov_b32_e32 v25, 0
	v_mov_b32_e32 v2, 0
	v_mov_b32_e32 v3, 0
	v_mov_b32_e32 v4, 0
	v_mov_b32_e32 v5, 0
	v_mov_b32_e32 v250, 0
	v_mov_b32_e32 v251, 0
	v_mov_b32_e32 v252, 0
	v_mov_b32_e32 v253, 0
	buffer_load_dwordx4 v[226:229], v242, s[20:23], 0 offen sc1
	buffer_load_dwordx4 v[230:233], v243, s[20:23], 0 offen sc1
	buffer_load_dwordx4 v[234:237], v244, s[20:23], 0 offen sc1
	buffer_load_dwordx4 v[238:241], v245, s[20:23], 0 offen sc1
	s_mov_b64 s[26:27], s[24:25]
	s_cmp_eq_u64 s[2:3], 0
	s_cbranch_scc1 .Lrec_noflush
	s_and_b32 s29, s46, 3
	s_cmp_lg_u32 s29, 0
	s_cbranch_scc1 .Lrec_noflush
	s_cmp_lt_u32 s46, 4
	s_cbranch_scc1 .Lrec_noflush
	s_add_i32 s29, s46, -4
	v_accvgpr_read_b32 v46, a94
	v_or_b32_e32 v50, s29, v46
	v_lshlrev_b32_e32 v46, 3, v50
	v_accvgpr_read_b32 v47, a95
	v_and_or_b32 v46, v46, 40, v47
	v_accvgpr_read_b32 v47, a96
	v_lshl_add_u32 v47, v47, 1, 0
	v_lshl_add_u32 v54, v46, 6, v47
	ds_read_b128 v[46:49], v54 offset:33024
	v_ashrrev_i32_e32 v51, 31, v50
	v_accvgpr_read_b32 v52, a100
	v_lshlrev_b64 v[50:51], 17, v[50:51]
	v_accvgpr_read_b32 v53, a101
	v_lshl_add_u64 v[50:51], v[52:53], 0, v[50:51]
	v_add_co_u32_e32 v52, vcc, 0x20000, v50
	s_nop 1
	v_addc_co_u32_e32 v53, vcc, 0, v51, vcc
	s_waitcnt lgkmcnt(0)
	global_store_dwordx4 v[52:53], v[46:49], off
	s_nop 1
	ds_read_b128 v[46:49], v54 offset:34048
	v_add_co_u32_e32 v50, vcc, 0x60000, v50
	s_nop 1
	v_addc_co_u32_e32 v51, vcc, 0, v51, vcc
	s_waitcnt lgkmcnt(0)
	global_store_dwordx4 v[50:51], v[46:49], off
	s_nop 1
.Lrec_noflush:
	v_mov_b32_e32 v46, 0
	v_mov_b32_e32 v47, 0
	v_mov_b32_e32 v48, 0
	v_mov_b32_e32 v49, 0
	v_mov_b32_e32 v50, 0
	v_mov_b32_e32 v51, 0
	v_mov_b32_e32 v52, 0
	v_mov_b32_e32 v53, 0
	s_sleep 4
	buffer_load_dwordx4 v[194:197], v242, s[20:23], 0 offen sc1
	buffer_load_dwordx4 v[198:201], v243, s[20:23], 0 offen sc1
	buffer_load_dwordx4 v[202:205], v244, s[20:23], 0 offen sc1
	buffer_load_dwordx4 v[206:209], v245, s[20:23], 0 offen sc1
	s_mov_b32 s46, s14
	s_branch .Lrec_step

.Lrec_retry0:
	s_add_i32 s14, s14, 1
	s_cmp_gt_u32 s14, 0x40000
	s_cbranch_scc1 .Lrec_dead0
	buffer_load_dwordx4 v[194:197], v242, s[20:23], 0 offen sc1
	buffer_load_dwordx4 v[198:201], v243, s[20:23], 0 offen sc1
	buffer_load_dwordx4 v[202:205], v244, s[20:23], 0 offen sc1
	buffer_load_dwordx4 v[206:209], v245, s[20:23], 0 offen sc1
	s_branch .Lrec_b0

.Lrec_retry1:
	s_add_i32 s14, s14, 1
	s_cmp_gt_u32 s14, 0x40000
	s_cbranch_scc1 .Lrec_dead1
	buffer_load_dwordx4 v[198:201], v243, s[20:23], 0 offen sc1
	buffer_load_dwordx4 v[202:205], v244, s[20:23], 0 offen sc1
	buffer_load_dwordx4 v[206:209], v245, s[20:23], 0 offen sc1
	s_branch .Lrec_b1

.Lrec_retry2:
	s_add_i32 s14, s14, 1
	s_cmp_gt_u32 s14, 0x40000
	s_cbranch_scc1 .Lrec_dead2
	buffer_load_dwordx4 v[202:205], v244, s[20:23], 0 offen sc1
	buffer_load_dwordx4 v[206:209], v245, s[20:23], 0 offen sc1
	s_branch .Lrec_b2

.Lrec_retry3:
	s_add_i32 s14, s14, 1
	s_cmp_gt_u32 s14, 0x40000
	s_cbranch_scc1 .Lrec_dead3
	buffer_load_dwordx4 v[206:209], v245, s[20:23], 0 offen sc1
	s_branch .Lrec_b3

	.amdhsa_kernel _Z5k_recPKDF16_S0_PKfS0_jjS2_PfS3_PDF16_Pj
		.amdhsa_group_segment_fixed_size 0
		.amdhsa_private_segment_fixed_size 0
		.amdhsa_kernarg_size 80
		.amdhsa_user_sgpr_count 2
		.amdhsa_user_sgpr_dispatch_ptr 0
		.amdhsa_user_sgpr_queue_ptr 0
		.amdhsa_user_sgpr_kernarg_segment_ptr 1
		.amdhsa_user_sgpr_dispatch_id 0
		.amdhsa_user_sgpr_kernarg_preload_length 0
		.amdhsa_user_sgpr_kernarg_preload_offset 0
		.amdhsa_user_sgpr_private_segment_size 0
		.amdhsa_uses_dynamic_stack 0
		.amdhsa_enable_private_segment 0
		.amdhsa_system_sgpr_workgroup_id_x 1
		.amdhsa_system_sgpr_workgroup_id_y 0
		.amdhsa_system_sgpr_workgroup_id_z 0
		.amdhsa_system_sgpr_workgroup_info 0
		.amdhsa_system_vgpr_workitem_id 0
		.amdhsa_next_free_vgpr 432
		.amdhsa_next_free_sgpr 50
		.amdhsa_accum_offset 256
		.amdhsa_reserve_vcc 1
		.amdhsa_float_round_mode_32 0
		.amdhsa_float_round_mode_16_64 0
		.amdhsa_float_denorm_mode_32 3
		.amdhsa_float_denorm_mode_16_64 3
		.amdhsa_dx10_clamp 1
		.amdhsa_ieee_mode 1
		.amdhsa_fp16_overflow 0
		.amdhsa_tg_split 0
		.amdhsa_exception_fp_ieee_invalid_op 0
		.amdhsa_exception_fp_denorm_src 0
		.amdhsa_exception_fp_ieee_div_zero 0
		.amdhsa_exception_fp_ieee_overflow 0
		.amdhsa_exception_fp_ieee_underflow 0
		.amdhsa_exception_fp_ieee_inexact 0
		.amdhsa_exception_int_div_zero 0
	.end_amdhsa_kernel

amdhsa.kernels:
  - .agpr_count:     0
    .args:
      - .offset:         0
        .size:           288
        .value_kind:     by_value
    .group_segment_fixed_size: 16640
    .kernarg_segment_align: 8
    .kernarg_segment_size: 288
    .language:       OpenCL C
    .language_version:
      - 2
      - 0
    .max_flat_workgroup_size: 1024
    .name:           _Z8k_wt_all6WtJobs
    .private_segment_fixed_size: 0
    .sgpr_count:     30
    .sgpr_spill_count: 0
    .symbol:         _Z8k_wt_all6WtJobs.kd
    .uniform_work_group_size: 1
    .uses_dynamic_stack: false
    .vgpr_count:     44
    .vgpr_spill_count: 0
    .wavefront_size: 64
  - .agpr_count:     0
    .args:
      - .actual_access:  read_only
        .address_space:  global
        .offset:         0
        .size:           8
        .value_kind:     global_buffer
      - .actual_access:  read_only
        .address_space:  global
        .offset:         8
        .size:           8
        .value_kind:     global_buffer
      - .actual_access:  write_only
        .address_space:  global
        .offset:         16
        .size:           8
        .value_kind:     global_buffer
    .group_segment_fixed_size: 0
    .kernarg_segment_align: 8
    .kernarg_segment_size: 24
    .language:       OpenCL C
    .language_version:
      - 2
      - 0
    .max_flat_workgroup_size: 1024
    .name:           _Z8k_prepA1PKfS0_PDF16_
    .private_segment_fixed_size: 0
    .sgpr_count:     16
    .sgpr_spill_count: 0
    .symbol:         _Z8k_prepA1PKfS0_PDF16_.kd
    .uniform_work_group_size: 1
    .uses_dynamic_stack: false
    .vgpr_count:     15
    .vgpr_spill_count: 0
    .wavefront_size: 64
  - .agpr_count:     0
    .args:
      - .actual_access:  read_only
        .address_space:  global
        .offset:         0
        .size:           8
        .value_kind:     global_buffer
      - .actual_access:  read_only
        .address_space:  global
        .offset:         8
        .size:           8
        .value_kind:     global_buffer
      - .actual_access:  read_only
        .address_space:  global
        .offset:         16
        .size:           8
        .value_kind:     global_buffer
      - .actual_access:  write_only
        .address_space:  global
        .offset:         24
        .size:           8
        .value_kind:     global_buffer
    .group_segment_fixed_size: 4096
    .kernarg_segment_align: 8
    .kernarg_segment_size: 32
    .language:       OpenCL C
    .language_version:
      - 2
      - 0
    .max_flat_workgroup_size: 1024
    .name:           _Z7k_bias0PKfPKiS0_Pf
    .private_segment_fixed_size: 0
    .sgpr_count:     28
    .sgpr_spill_count: 0
    .symbol:         _Z7k_bias0PKfPKiS0_Pf.kd
    .uniform_work_group_size: 1
    .uses_dynamic_stack: false
    .vgpr_count:     78
    .vgpr_spill_count: 0
    .wavefront_size: 64
  - .agpr_count:     0
    .args:
      - .actual_access:  read_only
        .address_space:  global
        .offset:         0
        .size:           8
        .value_kind:     global_buffer
      - .actual_access:  read_only
        .address_space:  global
        .offset:         8
        .size:           8
        .value_kind:     global_buffer
      - .actual_access:  read_only
        .address_space:  global
        .offset:         16
        .size:           8
        .value_kind:     global_buffer
      - .actual_access:  read_only
        .address_space:  global
        .offset:         24
        .size:           8
        .value_kind:     global_buffer
      - .actual_access:  read_only
        .address_space:  global
        .offset:         32
        .size:           8
        .value_kind:     global_buffer
      - .actual_access:  write_only
        .address_space:  global
        .offset:         40
        .size:           8
        .value_kind:     global_buffer
    .group_segment_fixed_size: 0
    .kernarg_segment_align: 8
    .kernarg_segment_size: 48
    .language:       OpenCL C
    .language_version:
      - 2
      - 0
    .max_flat_workgroup_size: 1024
    .name:           _Z7k_biasLPKfS0_S0_S0_S0_Pf
    .private_segment_fixed_size: 0
    .sgpr_count:     24
    .sgpr_spill_count: 0
    .symbol:         _Z7k_biasLPKfS0_S0_S0_S0_Pf.kd
    .uniform_work_group_size: 1
    .uses_dynamic_stack: false
    .vgpr_count:     29
    .vgpr_spill_count: 0
    .wavefront_size: 64
  - .agpr_count:     0
    .args:
      - .actual_access:  read_only
        .address_space:  global
        .offset:         0
        .size:           8
        .value_kind:     global_buffer
      - .actual_access:  read_only
        .address_space:  global
        .offset:         8
        .size:           8
        .value_kind:     global_buffer
      - .actual_access:  write_only
        .address_space:  global
        .offset:         16
        .size:           8
        .value_kind:     global_buffer
      - .actual_access:  write_only
        .address_space:  global
        .offset:         24
        .size:           8
        .value_kind:     global_buffer
    .group_segment_fixed_size: 0
    .kernarg_segment_align: 8
    .kernarg_segment_size: 32
    .language:       OpenCL C
    .language_version:
      - 2
      - 0
    .max_flat_workgroup_size: 1024
    .name:           _Z8k_state0PKfS0_PDF16_Pf
    .private_segment_fixed_size: 0
    .sgpr_count:     18
    .sgpr_spill_count: 0
    .symbol:         _Z8k_state0PKfS0_PDF16_Pf.kd
    .uniform_work_group_size: 1
    .uses_dynamic_stack: false
    .vgpr_count:     7
    .vgpr_spill_count: 0
    .wavefront_size: 64
  - .agpr_count:     176
    .args:
      - .actual_access:  read_only
        .address_space:  global
        .offset:         0
        .size:           8
        .value_kind:     global_buffer
      - .actual_access:  read_only
        .address_space:  global
        .offset:         8
        .size:           8
        .value_kind:     global_buffer
      - .actual_access:  read_only
        .address_space:  global
        .offset:         16
        .size:           8
        .value_kind:     global_buffer
      - .address_space:  global
        .offset:         24
        .size:           8
        .value_kind:     global_buffer
      - .offset:         32
        .size:           4
        .value_kind:     by_value
      - .offset:         36
        .size:           4
        .value_kind:     by_value
      - .address_space:  global
        .offset:         40
        .size:           8
        .value_kind:     global_buffer
      - .address_space:  global
        .offset:         48
        .size:           8
        .value_kind:     global_buffer
      - .address_space:  global
        .offset:         56
        .size:           8
        .value_kind:     global_buffer
      - .address_space:  global
        .offset:         64
        .size:           8
        .value_kind:     global_buffer
      - .address_space:  global
        .offset:         72
        .size:           8
        .value_kind:     global_buffer
    .group_segment_fixed_size: 0
    .kernarg_segment_align: 8
    .kernarg_segment_size: 80
    .language:       OpenCL C
    .language_version:
      - 2
      - 0
    .max_flat_workgroup_size: 256
    .name:           _Z5k_recPKDF16_S0_PKfS0_jjS2_PfS3_PDF16_Pj
    .private_segment_fixed_size: 0
    .sgpr_count:     56
    .sgpr_spill_count: 0
    .symbol:         _Z5k_recPKDF16_S0_PKfS0_jjS2_PfS3_PDF16_Pj.kd
    .uniform_work_group_size: 1
    .uses_dynamic_stack: false
    .vgpr_count:     432
    .vgpr_spill_count: 0
    .wavefront_size: 64
  - .agpr_count:     0
    .args:
      - .address_space:  global
        .offset:         0
        .size:           8
        .value_kind:     global_buffer
    .group_segment_fixed_size: 0
    .kernarg_segment_align: 8
    .kernarg_segment_size: 8
    .language:       OpenCL C
    .language_version:
      - 2
      - 0
    .max_flat_workgroup_size: 1024
    .name:           _Z9k_softmaxPf
    .private_segment_fixed_size: 0
    .sgpr_count:     9
    .sgpr_spill_count: 0
    .symbol:         _Z9k_softmaxPf.kd
    .uniform_work_group_size: 1
    .uses_dynamic_stack: false
    .vgpr_count:     32
    .vgpr_spill_count: 0
    .wavefront_size: 64
  - .agpr_count:     0
    .args:
      - .address_space:  global
        .offset:         0
        .size:           8
        .value_kind:     global_buffer
      - .address_space:  global
        .offset:         8
        .size:           8
        .value_kind:     global_buffer
      - .actual_access:  write_only
        .address_space:  global
        .offset:         16
        .size:           8
        .value_kind:     global_buffer
      - .actual_access:  read_only
        .address_space:  global
        .offset:         24
        .size:           8
        .value_kind:     global_buffer
    .group_segment_fixed_size: 0
    .kernarg_segment_align: 8
    .kernarg_segment_size: 32
    .language:       OpenCL C
    .language_version:
      - 2
      - 0
    .max_flat_workgroup_size: 512
    .name:           _Z6k_gemmILi16384ELi4096ELi2048ELi0EEvPKDF16_S1_PvPKf
    .private_segment_fixed_size: 0
    .sgpr_count:     25
    .sgpr_spill_count: 0
    .symbol:         _Z6k_gemmILi16384ELi4096ELi2048ELi0EEvPKDF16_S1_PvPKf.kd
    .uniform_work_group_size: 1
    .uses_dynamic_stack: false
    .vgpr_count:     244
    .vgpr_spill_count: 0
    .wavefront_size: 64
  - .agpr_count:     0
    .args:
      - .address_space:  global
        .offset:         0
        .size:           8
        .value_kind:     global_buffer
      - .address_space:  global
        .offset:         8
        .size:           8
        .value_kind:     global_buffer
      - .actual_access:  write_only
        .address_space:  global
        .offset:         16
        .size:           8
        .value_kind:     global_buffer
      - .actual_access:  read_only
        .address_space:  global
        .offset:         24
        .size:           8
        .value_kind:     global_buffer
    .group_segment_fixed_size: 0
    .kernarg_segment_align: 8
    .kernarg_segment_size: 32
    .language:       OpenCL C
    .language_version:
      - 2
      - 0
    .max_flat_workgroup_size: 512
    .name:           _Z6k_gemmILi16384ELi4096ELi1024ELi0EEvPKDF16_S1_PvPKf
    .private_segment_fixed_size: 0
    .sgpr_count:     26
    .sgpr_spill_count: 0
    .symbol:         _Z6k_gemmILi16384ELi4096ELi1024ELi0EEvPKDF16_S1_PvPKf.kd
    .uniform_work_group_size: 1
    .uses_dynamic_stack: false
    .vgpr_count:     244
    .vgpr_spill_count: 0
    .wavefront_size: 64
  - .agpr_count:     0
    .args:
      - .address_space:  global
        .offset:         0
        .size:           8
        .value_kind:     global_buffer
      - .address_space:  global
        .offset:         8
        .size:           8
        .value_kind:     global_buffer
      - .actual_access:  write_only
        .address_space:  global
        .offset:         16
        .size:           8
        .value_kind:     global_buffer
      - .actual_access:  read_only
        .address_space:  global
        .offset:         24
        .size:           8
        .value_kind:     global_buffer
    .group_segment_fixed_size: 0
    .kernarg_segment_align: 8
    .kernarg_segment_size: 32
    .language:       OpenCL C
    .language_version:
      - 2
      - 0
    .max_flat_workgroup_size: 512
    .name:           _Z6k_gemmILi16384ELi1024ELi1024ELi1EEvPKDF16_S1_PvPKf
    .private_segment_fixed_size: 0
    .sgpr_count:     28
    .sgpr_spill_count: 0
    .symbol:         _Z6k_gemmILi16384ELi1024ELi1024ELi1EEvPKDF16_S1_PvPKf.kd
    .uniform_work_group_size: 1
    .uses_dynamic_stack: false
    .vgpr_count:     246
    .vgpr_spill_count: 0
    .wavefront_size: 64
